# P2c oa_finish: nt hint on the read-once o / z row loads
# baseline (speedup 1.0000x reference)
.LBB0_1298:
	s_abs_i32 s24, s34
	s_mul_hi_u32 s25, s24, s33
	s_mul_i32 s26, s25, s3
	s_ashr_i32 s1, s34, 31
	s_sub_i32 s24, s24, s26
	s_xor_b32 s1, s1, s93
	s_add_i32 s26, s25, 1
	s_sub_i32 s27, s24, s3
	s_cmp_ge_u32 s24, s3
	s_cselect_b32 s25, s26, s25
	s_cselect_b32 s24, s27, s24
	s_add_i32 s26, s25, 1
	s_cmp_ge_u32 s24, s3
	s_cselect_b32 s24, s26, s25
	s_xor_b32 s24, s24, s1
	s_sub_i32 s1, s24, s1
	s_cmp_gt_i32 s1, 0
	s_cselect_b64 s[30:31], -1, 0
	s_cmp_lt_i32 s1, 1
	v_lshl_add_u64 v[46:47], s[8:9], 0, v[42:43]
	s_cbranch_scc1 .LBB0_1300
	s_waitcnt vmcnt(2)
	v_lshl_add_u64 v[2:3], s[4:5], 0, v[42:43]
	global_load_dwordx4 v[38:41], v[46:47], off nt
	global_load_dwordx4 v[34:37], v[2:3], off nt
.LBB0_1300:
	s_cmp_gt_i32 s1, 1
	s_cselect_b64 s[28:29], -1, 0
	s_cmp_lt_i32 s1, 2
	s_cbranch_scc1 .LBB0_1302
	s_waitcnt vmcnt(2)
	v_lshl_add_u64 v[4:5], s[14:15], 0, v[42:43]
	v_lshl_add_u64 v[2:3], s[12:13], 0, v[42:43]
	global_load_dwordx4 v[30:33], v[4:5], off nt
	global_load_dwordx4 v[26:29], v[2:3], off nt
.LBB0_1302:
	s_cmp_gt_i32 s1, 2
	s_cselect_b64 s[26:27], -1, 0
	s_cmp_lt_i32 s1, 3
	s_cbranch_scc1 .LBB0_1304
	s_waitcnt vmcnt(2)
	v_lshl_add_u64 v[2:3], s[18:19], 0, v[42:43]
	global_load_dwordx4 v[22:25], v[2:3], off nt
	v_lshl_add_u64 v[2:3], s[16:17], 0, v[42:43]
	global_load_dwordx4 v[18:21], v[2:3], off nt
.LBB0_1304:
	s_cmp_gt_i32 s1, 3
	s_cselect_b64 s[24:25], -1, 0
	s_cmp_lt_i32 s1, 4
	s_cbranch_scc1 .LBB0_1306
	s_waitcnt vmcnt(2)
	v_lshl_add_u64 v[2:3], s[22:23], 0, v[42:43]
	global_load_dwordx4 v[14:17], v[2:3], off nt
	v_lshl_add_u64 v[2:3], s[20:21], 0, v[42:43]
	global_load_dwordx4 v[2:5], v[2:3], off nt
	s_nop 0
	global_load_dwordx4 v[6:9], v[44:45], off offset:16
	global_load_dwordx4 v[10:13], v[44:45], off
	s_andn2_b64 vcc, exec, s[30:31]
	s_cbranch_vccz .LBB0_1307
	s_branch .LBB0_1308
